# P7 router weights LDS layout permuted so the expert loop's ds_read_b128 have a 16-byte lane stride (no 2-way bank conflicts); on top of router loop rewrite
# speedup vs baseline: 1.0024x; 1.0007x over previous
; #define GAS __attribute__((address_space(1)))
; __device__ __forceinline__ void ln1_router_phase(const Args& a, Frame& F, int l) {
;     ...
;     { f32x4 wv[16];
; #pragma unroll
;       for (int k = 0; k < 16; ++k) wv[k] = *(const GAS f32x4*)(wr + 4 * (F.tid + NTHR * k));
; #pragma unroll
;       for (int k = 0; k < 16; ++k) { const int i4 = F.tid + NTHR * k, c = i4 >> 2, e0 = (i4 & 3) * 4;
; #pragma unroll
;           for (int j = 0; j < 4; ++j) wl[(e0 + j) * DM + c] = wv[k][j]; } }
.LBB0_795:
	v_readlane_b32 s0, v249, 5
	v_readlane_b32 s1, v249, 6
	s_cmp_le_i32 s0, s8
	s_cselect_b64 s[0:1], -1, 0
	s_and_b64 s[4:5], s[0:1], s[2:3]
	s_andn2_b64 vcc, exec, s[4:5]
	s_cbranch_vccnz .LBB0_940
	s_mov_b32 s0, -1
	s_nop 0
	v_mbcnt_lo_u32_b32 v0, s0, 0
	v_mbcnt_hi_u32_b32 v0, s0, v0
	v_readlane_b32 s0, v249, 4
	s_waitcnt vmcnt(0)
	s_nop 0
	v_add_u32_e32 v66, s0, v0
	v_readlane_b32 s0, v247, 30
	s_nop 0
	v_lshlrev_b32_e32 v68, 2, v66
	v_mov_b32_e32 v0, s0
	s_waitcnt lgkmcnt(0)
	ds_read_b64 v[2:3], v0
	v_readlane_b32 s0, v247, 43
	v_ashrrev_i32_e32 v69, 31, v68
	v_add_u32_e32 v6, 0x800, v68
	v_mov_b32_e32 v0, s0
	s_waitcnt lgkmcnt(0)
	v_readfirstlane_b32 s62, v2
	v_readfirstlane_b32 s63, v3
	ds_read_b128 v[2:5], v0
	v_readlane_b32 s0, v247, 44
	v_ashrrev_i32_e32 v7, 31, v6
	v_add_u32_e32 v10, 0x1000, v68
	v_mov_b32_e32 v0, s0
	s_waitcnt lgkmcnt(0)
	v_readfirstlane_b32 s8, v2
	v_readfirstlane_b32 s10, v3
	v_readfirstlane_b32 s2, v4
	v_readfirstlane_b32 s3, v5
	ds_read_b128 v[2:5], v0
	v_ashrrev_i32_e32 v11, 31, v10
	v_add_u32_e32 v14, 0x1800, v68
	v_ashrrev_i32_e32 v15, 31, v14
	v_add_u32_e32 v18, 0x2000, v68
	s_waitcnt lgkmcnt(0)
	v_readfirstlane_b32 s0, v2
	v_readfirstlane_b32 s1, v3
	v_readfirstlane_b32 s28, v4
	v_readfirstlane_b32 s29, v5
	v_lshl_add_u64 v[2:3], v[68:69], 2, s[0:1]
	global_load_dwordx4 v[2:5], v[2:3], off
	v_lshl_add_u64 v[6:7], v[6:7], 2, s[0:1]
	global_load_dwordx4 v[6:9], v[6:7], off
	v_lshl_add_u64 v[10:11], v[10:11], 2, s[0:1]
	global_load_dwordx4 v[10:13], v[10:11], off
	v_lshl_add_u64 v[14:15], v[14:15], 2, s[0:1]
	global_load_dwordx4 v[14:17], v[14:15], off
	v_ashrrev_i32_e32 v19, 31, v18
	v_lshl_add_u64 v[18:19], v[18:19], 2, s[0:1]
	global_load_dwordx4 v[18:21], v[18:19], off
	v_add_u32_e32 v22, 0x2800, v68
	v_ashrrev_i32_e32 v23, 31, v22
	v_lshl_add_u64 v[22:23], v[22:23], 2, s[0:1]
	global_load_dwordx4 v[22:25], v[22:23], off
	v_add_u32_e32 v26, 0x3000, v68
	v_ashrrev_i32_e32 v27, 31, v26
	v_lshl_add_u64 v[26:27], v[26:27], 2, s[0:1]
	global_load_dwordx4 v[38:41], v[26:27], off
	v_add_u32_e32 v26, 0x3800, v68
	v_ashrrev_i32_e32 v27, 31, v26
	v_lshl_add_u64 v[26:27], v[26:27], 2, s[0:1]
	global_load_dwordx4 v[62:65], v[26:27], off
	v_add_u32_e32 v26, 0x4000, v68
	v_ashrrev_i32_e32 v27, 31, v26
	v_lshl_add_u64 v[26:27], v[26:27], 2, s[0:1]
	global_load_dwordx4 v[58:61], v[26:27], off
	v_add_u32_e32 v26, 0x4800, v68
	v_ashrrev_i32_e32 v27, 31, v26
	v_lshl_add_u64 v[26:27], v[26:27], 2, s[0:1]
	global_load_dwordx4 v[54:57], v[26:27], off
	v_add_u32_e32 v26, 0x5000, v68
	v_ashrrev_i32_e32 v27, 31, v26
	v_lshl_add_u64 v[26:27], v[26:27], 2, s[0:1]
	global_load_dwordx4 v[50:53], v[26:27], off
	v_add_u32_e32 v26, 0x5800, v68
	v_ashrrev_i32_e32 v27, 31, v26
	v_lshl_add_u64 v[26:27], v[26:27], 2, s[0:1]
	global_load_dwordx4 v[46:49], v[26:27], off
	v_add_u32_e32 v26, 0x6000, v68
	v_ashrrev_i32_e32 v27, 31, v26
	v_lshl_add_u64 v[26:27], v[26:27], 2, s[0:1]
	global_load_dwordx4 v[42:45], v[26:27], off
	v_add_u32_e32 v26, 0x6800, v68
	v_ashrrev_i32_e32 v27, 31, v26
	v_lshl_add_u64 v[26:27], v[26:27], 2, s[0:1]
	global_load_dwordx4 v[34:37], v[26:27], off
	v_add_u32_e32 v26, 0x7000, v68
	v_ashrrev_i32_e32 v27, 31, v26
	v_lshl_add_u64 v[26:27], v[26:27], 2, s[0:1]
	global_load_dwordx4 v[30:33], v[26:27], off
	v_add_u32_e32 v26, 0x7800, v68
	v_ashrrev_i32_e32 v27, 31, v26
	v_lshl_add_u64 v[26:27], v[26:27], 2, s[0:1]
	global_load_dwordx4 v[26:29], v[26:27], off
	v_lshlrev_b32_e32 v67, 15, v66
	v_and_b32_e32 v0, -4, v66
	v_and_b32_e32 v67, 0x18000, v67
	v_and_b32_e32 v218, 0x7e0, v0
	v_and_b32_e32 v219, 16, v0
	v_lshrrev_b32_e32 v218, 1, v218
	v_lshlrev_b32_e32 v219, 6, v219
	v_and_b32_e32 v0, 0x180f, v0
	v_or3_b32 v0, v0, v218, v219
	v_add3_u32 v0, 0, v0, v67
	v_readlane_b32 s0, v248, 54
	v_readlane_b32 s1, v248, 55
	v_readfirstlane_b32 s11, v66
	s_waitcnt vmcnt(15)
	ds_write2st64_b32 v0, v2, v3 offset1:32
	ds_write2st64_b32 v0, v4, v5 offset0:64 offset1:96
	v_add_u32_e32 v0, 0x200, v66
	v_and_b32_e32 v0, -4, v0
	v_and_b32_e32 v218, 0x7e0, v0
	v_and_b32_e32 v219, 16, v0
	v_lshrrev_b32_e32 v218, 1, v218
	v_lshlrev_b32_e32 v219, 6, v219
	v_and_b32_e32 v0, 0x180f, v0
	v_or3_b32 v0, v0, v218, v219
	v_add3_u32 v0, 0, v0, v67
	s_waitcnt vmcnt(14)
	ds_write2st64_b32 v0, v6, v7 offset1:32
	ds_write2st64_b32 v0, v8, v9 offset0:64 offset1:96
	v_add_u32_e32 v0, 0x400, v66
	v_and_b32_e32 v0, -4, v0
	v_and_b32_e32 v218, 0x7e0, v0
	v_and_b32_e32 v219, 16, v0
	v_lshrrev_b32_e32 v218, 1, v218
	v_lshlrev_b32_e32 v219, 6, v219
	v_and_b32_e32 v0, 0x180f, v0
	v_or3_b32 v0, v0, v218, v219
	v_add3_u32 v0, 0, v0, v67
	s_waitcnt vmcnt(13)
	ds_write2st64_b32 v0, v10, v11 offset1:32
	ds_write2st64_b32 v0, v12, v13 offset0:64 offset1:96
	v_add_u32_e32 v0, 0x600, v66
	v_and_b32_e32 v0, -4, v0
	v_and_b32_e32 v218, 0x7e0, v0
	v_and_b32_e32 v219, 16, v0
	v_lshrrev_b32_e32 v218, 1, v218
	v_lshlrev_b32_e32 v219, 6, v219
	v_and_b32_e32 v0, 0x180f, v0
	v_or3_b32 v0, v0, v218, v219
	v_add3_u32 v0, 0, v0, v67
	s_waitcnt vmcnt(12)
	ds_write2st64_b32 v0, v14, v15 offset1:32
	ds_write2st64_b32 v0, v16, v17 offset0:64 offset1:96
	v_add_u32_e32 v0, 0x800, v66
	v_and_b32_e32 v0, -4, v0
	v_and_b32_e32 v218, 0x7e0, v0
	v_and_b32_e32 v219, 16, v0
	v_lshrrev_b32_e32 v218, 1, v218
	v_lshlrev_b32_e32 v219, 6, v219
	v_and_b32_e32 v0, 0x180f, v0
	v_or3_b32 v0, v0, v218, v219
	v_add3_u32 v0, 0, v0, v67
	s_waitcnt vmcnt(11)
	ds_write2st64_b32 v0, v18, v19 offset1:32
	ds_write2st64_b32 v0, v20, v21 offset0:64 offset1:96
	v_add_u32_e32 v0, 0xa00, v66
	v_and_b32_e32 v0, -4, v0
	v_and_b32_e32 v218, 0x7e0, v0
	v_and_b32_e32 v219, 16, v0
	v_lshrrev_b32_e32 v218, 1, v218
	v_lshlrev_b32_e32 v219, 6, v219
	v_and_b32_e32 v0, 0x180f, v0
	v_or3_b32 v0, v0, v218, v219
	v_add3_u32 v0, 0, v0, v67
	s_waitcnt vmcnt(10)
; __device__ __forceinline__ void ln1_router_phase(const Args& a, Frame& F, int l) {
;     ...
;       for (int k = 0; k < 16; ++k) { const int i4 = F.tid + NTHR * k, c = i4 >> 2, e0 = (i4 & 3) * 4;
; #pragma unroll
;           for (int j = 0; j < 4; ++j) wl[(e0 + j) * DM + c] = wv[k][j]; } }
;     __syncthreads();
	ds_write2st64_b32 v0, v22, v23 offset1:32
	ds_write2st64_b32 v0, v24, v25 offset0:64 offset1:96
	v_add_u32_e32 v0, 0xc00, v66
	v_and_b32_e32 v0, -4, v0
	v_and_b32_e32 v218, 0x7e0, v0
	v_and_b32_e32 v219, 16, v0
	v_lshrrev_b32_e32 v218, 1, v218
	v_lshlrev_b32_e32 v219, 6, v219
	v_and_b32_e32 v0, 0x180f, v0
	v_or3_b32 v0, v0, v218, v219
	v_add3_u32 v0, 0, v0, v67
	s_waitcnt vmcnt(9)
	ds_write2st64_b32 v0, v38, v39 offset1:32
	ds_write2st64_b32 v0, v40, v41 offset0:64 offset1:96
	v_add_u32_e32 v0, 0xe00, v66
	v_and_b32_e32 v0, -4, v0
	v_and_b32_e32 v218, 0x7e0, v0
	v_and_b32_e32 v219, 16, v0
	v_lshrrev_b32_e32 v218, 1, v218
	v_lshlrev_b32_e32 v219, 6, v219
	v_and_b32_e32 v0, 0x180f, v0
	v_or3_b32 v0, v0, v218, v219
	v_add3_u32 v0, 0, v0, v67
	s_waitcnt vmcnt(8)
	ds_write2st64_b32 v0, v62, v63 offset1:32
	ds_write2st64_b32 v0, v64, v65 offset0:64 offset1:96
	v_add_u32_e32 v0, 0x1000, v66
	v_and_b32_e32 v0, -4, v0
	v_and_b32_e32 v218, 0x7e0, v0
	v_and_b32_e32 v219, 16, v0
	v_lshrrev_b32_e32 v218, 1, v218
	v_lshlrev_b32_e32 v219, 6, v219
	v_and_b32_e32 v0, 0x180f, v0
	v_or3_b32 v0, v0, v218, v219
	v_add3_u32 v0, 0, v0, v67
	s_waitcnt vmcnt(7)
	ds_write2st64_b32 v0, v58, v59 offset1:32
	ds_write2st64_b32 v0, v60, v61 offset0:64 offset1:96
	v_add_u32_e32 v0, 0x1200, v66
	v_and_b32_e32 v0, -4, v0
	v_and_b32_e32 v218, 0x7e0, v0
	v_and_b32_e32 v219, 16, v0
	v_lshrrev_b32_e32 v218, 1, v218
	v_lshlrev_b32_e32 v219, 6, v219
	v_and_b32_e32 v0, 0x180f, v0
	v_or3_b32 v0, v0, v218, v219
	v_add3_u32 v0, 0, v0, v67
	s_waitcnt vmcnt(6)
	ds_write2st64_b32 v0, v54, v55 offset1:32
	ds_write2st64_b32 v0, v56, v57 offset0:64 offset1:96
	v_add_u32_e32 v0, 0x1400, v66
	v_and_b32_e32 v0, -4, v0
	v_and_b32_e32 v218, 0x7e0, v0
	v_and_b32_e32 v219, 16, v0
	v_lshrrev_b32_e32 v218, 1, v218
	v_lshlrev_b32_e32 v219, 6, v219
	v_and_b32_e32 v0, 0x180f, v0
	v_or3_b32 v0, v0, v218, v219
	v_add3_u32 v0, 0, v0, v67
	s_waitcnt vmcnt(5)
	ds_write2st64_b32 v0, v50, v51 offset1:32
	ds_write2st64_b32 v0, v52, v53 offset0:64 offset1:96
	v_add_u32_e32 v0, 0x1600, v66
	v_and_b32_e32 v0, -4, v0
	v_and_b32_e32 v218, 0x7e0, v0
	v_and_b32_e32 v219, 16, v0
	v_lshrrev_b32_e32 v218, 1, v218
	v_lshlrev_b32_e32 v219, 6, v219
	v_and_b32_e32 v0, 0x180f, v0
	v_or3_b32 v0, v0, v218, v219
	v_add3_u32 v0, 0, v0, v67
	s_waitcnt vmcnt(4)
	ds_write2st64_b32 v0, v46, v47 offset1:32
	ds_write2st64_b32 v0, v48, v49 offset0:64 offset1:96
	v_add_u32_e32 v0, 0x1800, v66
	v_and_b32_e32 v0, -4, v0
	v_and_b32_e32 v218, 0x7e0, v0
	v_and_b32_e32 v219, 16, v0
	v_lshrrev_b32_e32 v218, 1, v218
	v_lshlrev_b32_e32 v219, 6, v219
	v_and_b32_e32 v0, 0x180f, v0
	v_or3_b32 v0, v0, v218, v219
	v_add3_u32 v0, 0, v0, v67
	s_waitcnt vmcnt(3)
	ds_write2st64_b32 v0, v42, v43 offset1:32
	ds_write2st64_b32 v0, v44, v45 offset0:64 offset1:96
	v_add_u32_e32 v0, 0x1a00, v66
	v_and_b32_e32 v0, -4, v0
	v_and_b32_e32 v218, 0x7e0, v0
	v_and_b32_e32 v219, 16, v0
	v_lshrrev_b32_e32 v218, 1, v218
	v_lshlrev_b32_e32 v219, 6, v219
	v_and_b32_e32 v0, 0x180f, v0
	v_or3_b32 v0, v0, v218, v219
	v_add3_u32 v0, 0, v0, v67
	s_waitcnt vmcnt(2)
	ds_write2st64_b32 v0, v34, v35 offset1:32
	ds_write2st64_b32 v0, v36, v37 offset0:64 offset1:96
	v_add_u32_e32 v0, 0x1c00, v66
	v_and_b32_e32 v0, -4, v0
	v_and_b32_e32 v218, 0x7e0, v0
	v_and_b32_e32 v219, 16, v0
	v_lshrrev_b32_e32 v218, 1, v218
	v_lshlrev_b32_e32 v219, 6, v219
	v_and_b32_e32 v0, 0x180f, v0
	v_or3_b32 v0, v0, v218, v219
	v_add3_u32 v0, 0, v0, v67
	s_waitcnt vmcnt(1)
	ds_write2st64_b32 v0, v30, v31 offset1:32
	ds_write2st64_b32 v0, v32, v33 offset0:64 offset1:96
	v_add_u32_e32 v0, 0x1e00, v66
	v_and_b32_e32 v0, -4, v0
	v_and_b32_e32 v218, 0x7e0, v0
	v_and_b32_e32 v219, 16, v0
	v_lshrrev_b32_e32 v218, 1, v218
	v_lshlrev_b32_e32 v219, 6, v219
	v_and_b32_e32 v0, 0x180f, v0
	v_or3_b32 v0, v0, v218, v219
	v_add3_u32 v0, 0, v0, v67
	s_andn2_b64 vcc, exec, s[0:1]
	s_waitcnt vmcnt(0)
	ds_write2st64_b32 v0, v26, v27 offset1:32
	ds_write2st64_b32 v0, v28, v29 offset0:64 offset1:96
	s_waitcnt lgkmcnt(0)
	s_barrier
; #define LAS __attribute__((address_space(3)))
; __device__ __forceinline__ void ln1_router_phase(const Args& a, Frame& F, int l) {
;     ...
;     const int lane = F.lane; const int gw = F.bx * NWAVES + F.wave, NGW = F.G * NWAVES;
;     LAS int* asg_e = (LAS int*)(F.lds + LDSX_OFF); LAS int* asg_d = asg_e + 128; LAS float* asg_g = (LAS float*)(asg_e + 256); LAS int* wgcnt = asg_e + 384; LAS int* wgbase = asg_e + 400;
;     int* ldst = (int*)(F.ws + WS_LIST + (size_t)l * 2 * MiB); float* lgate = (float*)(F.ws + WS_LIST + (size_t)l * 2 * MiB + MiB);
;     const int niter = (T + NGW - 1) / NGW;
;     for (int it = 0; it < niter; it += 2) {
;         const int rowA = gw + it * NGW, rowB = gw + (it + 1) * NGW; const int slot = it & 7;
;         const bool okA = rowA < T, okB = (it + 1 < niter) && rowB < T; const int rA = okA ? rowA : 0, rB = okB ? rowB : rA;
;     ...
;             for (int j = 0; j < 4; ++j) { const f32x4 w0 = *(const LAS f32x4*)(wl + e * DM + 8 * lane + 512 * j), w1 = *(const LAS f32x4*)(wl + e * DM + 8 * lane + 512 * j + 4);
	s_cbranch_vccnz .LBB0_939
	v_and_b32_e32 v116, 63, v66
	v_lshlrev_b32_e32 v0, 4, v116
	v_lshl_add_u64 v[2:3], s[62:63], 0, v[0:1]
	v_and_b32_e32 v0, 64, v228
	v_add_u32_e32 v0, 64, v0
	v_xor_b32_e32 v4, 1, v228
	v_cmp_lt_i32_e32 vcc, v4, v0
	v_readlane_b32 s0, v246, 8
	v_readlane_b32 s1, v246, 9
	v_cndmask_b32_e32 v4, v228, v4, vcc
	v_lshlrev_b32_e32 v117, 2, v4
	v_xor_b32_e32 v4, 2, v228
	v_cmp_lt_i32_e32 vcc, v4, v0
	s_lshl_b32 s88, s0, 1
	s_ashr_i32 s16, s11, 6
	v_cndmask_b32_e32 v4, v228, v4, vcc
	v_lshlrev_b32_e32 v118, 2, v4
	v_xor_b32_e32 v4, 4, v228
	v_readlane_b32 s9, v247, 25
	v_cmp_lt_i32_e32 vcc, v4, v0
	s_mov_b32 s12, s0
	s_lshl_b64 s[0:1], s[88:89], 20
	s_add_i32 s68, s16, s9
	v_cndmask_b32_e32 v4, v228, v4, vcc
	s_add_u32 s0, s62, s0
	v_lshlrev_b32_e32 v119, 2, v4
	v_xor_b32_e32 v4, 8, v228
	s_addc_u32 s1, s63, s1
	v_cmp_lt_i32_e32 vcc, v4, v0
	s_add_u32 s64, s0, 0x100000
	s_addc_u32 s65, s1, 0
	v_cndmask_b32_e32 v4, v228, v4, vcc
	v_lshlrev_b32_e32 v120, 2, v4
	v_xor_b32_e32 v4, 16, v228
	s_add_u32 s66, s0, 0x200000
	v_cmp_lt_i32_e32 vcc, v4, v0
	s_addc_u32 s67, s1, 0
	s_lshl_b32 s0, s12, 6
	s_lshl_b64 s[12:13], s[88:89], 13
	v_cndmask_b32_e32 v4, v228, v4, vcc
	s_add_u32 s8, s8, s12
	v_lshlrev_b32_e32 v121, 2, v4
	v_xor_b32_e32 v4, 32, v228
	s_addc_u32 s9, s10, s13
	v_cmp_lt_i32_e32 vcc, v4, v0
	s_add_u32 s2, s2, s12
	s_addc_u32 s3, s3, s13
	v_cndmask_b32_e32 v0, v228, v4, vcc
	v_lshlrev_b32_e32 v122, 2, v0
	v_lshlrev_b32_e32 v0, 5, v116
	v_lshl_add_u64 v[8:9], s[8:9], 0, v[0:1]
	v_lshl_add_u64 v[10:11], s[2:3], 0, v[0:1]
	s_mov_b64 s[2:3], 0x1000
	v_lshl_add_u64 v[12:13], v[8:9], 0, s[2:3]
	v_lshl_add_u64 v[14:15], v[10:11], 0, s[2:3]
	s_mov_b64 s[2:3], 0x1800
	v_lshl_add_u64 v[16:17], v[8:9], 0, s[2:3]
	v_lshl_add_u64 v[18:19], v[10:11], 0, s[2:3]
	s_mov_b64 s[2:3], 0x6a800000
	v_lshl_add_u64 v[20:21], v[2:3], 0, s[2:3]
	s_mov_b64 s[2:3], 0x62800000
	s_mov_b32 s1, s89
	v_lshl_add_u64 v[22:23], v[2:3], 0, s[2:3]
	s_movk_i32 s2, 0x80
	v_cmp_gt_i32_e64 s[44:45], s2, v66
	s_add_i32 s2, 0, 0x20000
	s_lshl_b64 s[0:1], s[0:1], 2
	s_mov_b64 s[10:11], 0x5a800000
	s_add_u32 s0, s62, s0
	v_lshl_add_u64 v[6:7], v[2:3], 0, s[10:11]
	v_lshlrev_b32_e32 v2, 2, v228
	s_addc_u32 s1, s63, s1
	v_ashrrev_i32_e32 v67, 31, v66
	v_and_b32_e32 v123, 0x100, v2
	v_lshl_add_u64 v[2:3], v[66:67], 2, s[0:1]
	s_mov_b64 s[0:1], 0x8000
	v_lshl_add_u64 v[24:25], v[2:3], 0, s[0:1]
	v_readlane_b32 s0, v247, 46
	v_lshl_add_u32 v140, s16, 4, v116
	v_add_u32_e32 v139, s2, v68
	v_add_u32_e32 v142, s0, v68
	v_readlane_b32 s0, v247, 47
	v_add_u32_e32 v4, 2, v140
	v_readlane_b32 s2, v247, 45
	v_add_u32_e32 v143, s0, v68
	v_readlane_b32 s0, v247, 48
	s_mov_b32 s69, 0
	v_lshrrev_b32_e32 v0, 1, v0
	v_add_u32_e32 v0, 0, v0
	v_or_b32_e32 v124, 4, v123
	v_or_b32_e32 v125, 8, v123
	v_or_b32_e32 v126, 12, v123
	v_or_b32_e32 v127, 16, v123
	v_or_b32_e32 v128, 20, v123
	v_or_b32_e32 v129, 24, v123
	v_or_b32_e32 v130, 28, v123
	v_or_b32_e32 v131, 32, v123
	v_or_b32_e32 v132, 36, v123
	v_or_b32_e32 v133, 40, v123
	v_or_b32_e32 v134, 44, v123
	v_or_b32_e32 v135, 48, v123
	v_or_b32_e32 v136, 52, v123
	v_or_b32_e32 v137, 56, v123
	v_or_b32_e32 v138, 60, v123
	v_cmp_gt_u32_e64 s[40:41], 2, v116
	v_cmp_eq_u32_e64 s[42:43], 0, v116
	v_cmp_gt_i32_e64 s[46:47], 16, v66
	v_add_u32_e32 v141, s2, v68
	v_add_u32_e32 v144, s0, v68
	v_lshlrev_b32_e32 v145, 13, v116
	v_lshlrev_b32_e32 v146, 2, v4
	s_branch .LBB0_800

; #define LAS __attribute__((address_space(3)))
; __device__ __forceinline__ void ln1_router_phase(const Args& a, Frame& F, int l) {
;     ...
; #pragma unroll 1
;         for (int e = 0; e < 16; ++e) { float sA = 0.f, sB = 0.f;
; #pragma unroll
;             for (int j = 0; j < 4; ++j) { const f32x4 w0 = *(const LAS f32x4*)(wl + e * DM + 8 * lane + 512 * j), w1 = *(const LAS f32x4*)(wl + e * DM + 8 * lane + 512 * j + 4);
;                 sA += (va[j][0] * w0[0] + va[j][1] * w0[1]) + (va[j][2] * w0[2] + va[j][3] * w0[3]) + (va[j][4] * w1[0] + va[j][5] * w1[1]) + (va[j][6] * w1[2] + va[j][7] * w1[3]);
;                 sB += (vb[j][0] * w0[0] + vb[j][1] * w0[1]) + (vb[j][2] * w0[2] + vb[j][3] * w0[3]) + (vb[j][4] * w1[0] + vb[j][5] * w1[1]) + (vb[j][6] * w1[2] + vb[j][7] * w1[3]); }
;             sA = wave_sum(sA); sB = wave_sum(sB); lgA = (lane == e) ? sA : lgA; lgB = (lane == e) ? sB : lgB; }
.LBB0_808:
	s_nop 1
	v_mov_b32_e32 v86, 0
	s_mov_b32 s0, 0
	v_mov_b32_e32 v87, 0
	v_add_u32_e32 v99, s0, v0
	ds_read_b128 v[148:151], v99
	ds_read_b128 v[152:155], v99 offset:1024
	ds_read_b128 v[156:159], v99 offset:2048
	ds_read_b128 v[160:163], v99 offset:3072
	ds_read_b128 v[164:167], v99 offset:4096
	ds_read_b128 v[168:171], v99 offset:5120
	ds_read_b128 v[172:175], v99 offset:6144
	ds_read_b128 v[176:179], v99 offset:7168
.Lmy_rt_loop:
	v_cmp_eq_u32_e32 vcc, s0, v145
	s_addk_i32 s0, 0x2000
	v_add_u32_e32 v99, s0, v0
	ds_read_b128 v[180:183], v99
	ds_read_b128 v[184:187], v99 offset:1024
	ds_read_b128 v[188:191], v99 offset:2048
	ds_read_b128 v[200:203], v99 offset:3072
	ds_read_b128 v[204:207], v99 offset:4096
	ds_read_b128 v[208:211], v99 offset:5120
	ds_read_b128 v[212:215], v99 offset:6144
	ds_read_b128 v[92:95], v99 offset:7168
	s_waitcnt lgkmcnt(8)
	v_pk_mul_f32 v[96:97], v[2:3], v[148:149] op_sel:[0,1] op_sel_hi:[1,0]
	s_nop 0
	v_pk_fma_f32 v[148:149], v[26:27], v[148:149], v[96:97]
	v_pk_mul_f32 v[96:97], v[30:31], v[150:151] op_sel:[0,1] op_sel_hi:[1,0]
	s_nop 0
	v_pk_fma_f32 v[150:151], v[34:35], v[150:151], v[96:97]
	s_nop 0
	v_pk_add_f32 v[148:149], v[148:149], v[150:151]
	v_pk_mul_f32 v[150:151], v[4:5], v[152:153] op_sel:[0,1] op_sel_hi:[1,0]
	s_nop 0
	v_pk_fma_f32 v[150:151], v[28:29], v[152:153], v[150:151]
	s_nop 0
	v_pk_add_f32 v[148:149], v[148:149], v[150:151]
	v_pk_mul_f32 v[150:151], v[32:33], v[154:155] op_sel:[0,1] op_sel_hi:[1,0]
	s_nop 0
	v_pk_fma_f32 v[150:151], v[36:37], v[154:155], v[150:151]
	s_nop 0
	v_pk_add_f32 v[100:101], v[150:151], v[148:149]
	s_nop 0
	v_pk_add_f32 v[100:101], v[100:101], 0 op_sel_hi:[1,0]
	v_pk_mul_f32 v[96:97], v[38:39], v[156:157] op_sel:[0,1] op_sel_hi:[1,0]
	s_nop 0
	v_pk_fma_f32 v[156:157], v[42:43], v[156:157], v[96:97]
	v_pk_mul_f32 v[96:97], v[46:47], v[158:159] op_sel:[0,1] op_sel_hi:[1,0]
	s_nop 0
	v_pk_fma_f32 v[158:159], v[50:51], v[158:159], v[96:97]
	s_nop 0
	v_pk_add_f32 v[156:157], v[156:157], v[158:159]
	v_pk_mul_f32 v[158:159], v[40:41], v[160:161] op_sel:[0,1] op_sel_hi:[1,0]
	s_nop 0
	v_pk_fma_f32 v[158:159], v[44:45], v[160:161], v[158:159]
	s_nop 0
	v_pk_add_f32 v[102:103], v[156:157], v[158:159]
	v_pk_mul_f32 v[156:157], v[48:49], v[162:163] op_sel:[0,1] op_sel_hi:[1,0]
	s_nop 0
	v_pk_fma_f32 v[104:105], v[52:53], v[162:163], v[156:157]
	s_nop 0
	v_pk_add_f32 v[102:103], v[104:105], v[102:103]
	v_pk_mul_f32 v[96:97], v[54:55], v[164:165] op_sel:[0,1] op_sel_hi:[1,0]
	s_nop 0
	v_pk_fma_f32 v[164:165], v[58:59], v[164:165], v[96:97]
	v_pk_mul_f32 v[96:97], v[62:63], v[166:167] op_sel:[0,1] op_sel_hi:[1,0]
	v_pk_mul_f32 v[108:109], v[68:69], v[170:171]
	v_pk_fma_f32 v[166:167], v[66:67], v[166:167], v[96:97]
	v_pk_fma_f32 v[170:171], v[64:65], v[170:171], v[108:109] op_sel:[0,0,1] op_sel_hi:[1,1,0]
	v_pk_add_f32 v[106:107], v[164:165], v[166:167]
	v_pk_mul_f32 v[164:165], v[56:57], v[168:169] op_sel:[0,1] op_sel_hi:[1,0]
	v_pk_add_f32 v[100:101], v[100:101], v[102:103]
	v_pk_fma_f32 v[168:169], v[60:61], v[168:169], v[164:165]
	s_nop 0
	v_pk_add_f32 v[168:169], v[106:107], v[168:169]
	v_pk_mul_f32 v[110:111], v[70:71], v[172:173] op_sel:[0,1] op_sel_hi:[1,0]
	s_nop 0
	v_pk_fma_f32 v[172:173], v[74:75], v[172:173], v[110:111]
	v_pk_mul_f32 v[110:111], v[78:79], v[174:175] op_sel:[0,1] op_sel_hi:[1,0]
	v_pk_add_f32 v[168:169], v[170:171], v[168:169] op_sel:[0,1] op_sel_hi:[1,0]
	v_pk_fma_f32 v[174:175], v[82:83], v[174:175], v[110:111]
	v_pk_mul_f32 v[110:111], v[76:77], v[176:177]
	v_pk_add_f32 v[172:173], v[172:173], v[174:175]
	v_pk_fma_f32 v[174:175], v[72:73], v[176:177], v[110:111] op_sel:[0,0,1] op_sel_hi:[1,1,0]
	v_pk_add_f32 v[168:169], v[100:101], v[168:169] op_sel:[1,0] op_sel_hi:[0,1]
	v_pk_add_f32 v[172:173], v[172:173], v[174:175] op_sel:[1,0] op_sel_hi:[0,1]
	v_pk_mul_f32 v[174:175], v[84:85], v[178:179]
	s_nop 0
	v_pk_fma_f32 v[174:175], v[80:81], v[178:179], v[174:175] op_sel:[0,0,1] op_sel_hi:[1,1,0]
	s_nop 0
	v_pk_add_f32 v[172:173], v[174:175], v[172:173]
	s_nop 0
	v_pk_add_f32 v[88:89], v[168:169], v[172:173]
	s_nop 1
	v_add_f32_dpp v88, v88, v88 quad_perm:[1,0,3,2] row_mask:0xf bank_mask:0xf
	v_add_f32_dpp v89, v89, v89 quad_perm:[1,0,3,2] row_mask:0xf bank_mask:0xf
	s_nop 0
	v_add_f32_dpp v88, v88, v88 quad_perm:[2,3,0,1] row_mask:0xf bank_mask:0xf
	v_add_f32_dpp v89, v89, v89 quad_perm:[2,3,0,1] row_mask:0xf bank_mask:0xf
	s_nop 0
	v_add_f32_dpp v88, v88, v88 row_half_mirror row_mask:0xf bank_mask:0xf
	v_add_f32_dpp v89, v89, v89 row_half_mirror row_mask:0xf bank_mask:0xf
	s_nop 0
	v_add_f32_dpp v88, v88, v88 row_mirror row_mask:0xf bank_mask:0xf
	v_add_f32_dpp v89, v89, v89 row_mirror row_mask:0xf bank_mask:0xf
	v_mov_b32_e32 v90, v88
	v_mov_b32_e32 v91, v89
	s_nop 1
	v_permlane16_swap_b32_e32 v88, v90
	v_permlane16_swap_b32_e32 v89, v91
	v_add_f32_e32 v88, v88, v90
	v_add_f32_e32 v89, v89, v91
	v_mov_b32_e32 v90, v88
	v_mov_b32_e32 v91, v89
	s_nop 1
	v_permlane32_swap_b32_e32 v88, v90
	v_permlane32_swap_b32_e32 v89, v91
	v_add_f32_e32 v88, v88, v90
	v_add_f32_e32 v89, v89, v91
	v_cndmask_b32_e32 v86, v86, v88, vcc
	v_cndmask_b32_e32 v87, v87, v89, vcc
	v_cmp_eq_u32_e32 vcc, s0, v145
	s_addk_i32 s0, 0x2000
	v_add_u32_e32 v99, s0, v0
	ds_read_b128 v[148:151], v99
	ds_read_b128 v[152:155], v99 offset:1024
	ds_read_b128 v[156:159], v99 offset:2048
	ds_read_b128 v[160:163], v99 offset:3072
	ds_read_b128 v[164:167], v99 offset:4096
	ds_read_b128 v[168:171], v99 offset:5120
	ds_read_b128 v[172:175], v99 offset:6144
	ds_read_b128 v[176:179], v99 offset:7168
	s_waitcnt lgkmcnt(8)
; #define LAS __attribute__((address_space(3)))
; __device__ __forceinline__ void ln1_router_phase(const Args& a, Frame& F, int l) {
;     ...
; #pragma unroll 1
;         for (int e = 0; e < 16; ++e) { float sA = 0.f, sB = 0.f;
; #pragma unroll
;             for (int j = 0; j < 4; ++j) { const f32x4 w0 = *(const LAS f32x4*)(wl + e * DM + 8 * lane + 512 * j), w1 = *(const LAS f32x4*)(wl + e * DM + 8 * lane + 512 * j + 4);
;                 sA += (va[j][0] * w0[0] + va[j][1] * w0[1]) + (va[j][2] * w0[2] + va[j][3] * w0[3]) + (va[j][4] * w1[0] + va[j][5] * w1[1]) + (va[j][6] * w1[2] + va[j][7] * w1[3]);
;                 sB += (vb[j][0] * w0[0] + vb[j][1] * w0[1]) + (vb[j][2] * w0[2] + vb[j][3] * w0[3]) + (vb[j][4] * w1[0] + vb[j][5] * w1[1]) + (vb[j][6] * w1[2] + vb[j][7] * w1[3]); }
;             sA = wave_sum(sA); sB = wave_sum(sB); lgA = (lane == e) ? sA : lgA; lgB = (lane == e) ? sB : lgB; }
	v_pk_mul_f32 v[96:97], v[2:3], v[180:181] op_sel:[0,1] op_sel_hi:[1,0]
	s_nop 0
	v_pk_fma_f32 v[180:181], v[26:27], v[180:181], v[96:97]
	v_pk_mul_f32 v[96:97], v[30:31], v[182:183] op_sel:[0,1] op_sel_hi:[1,0]
	s_nop 0
	v_pk_fma_f32 v[182:183], v[34:35], v[182:183], v[96:97]
	s_nop 0
	v_pk_add_f32 v[180:181], v[180:181], v[182:183]
	v_pk_mul_f32 v[182:183], v[4:5], v[184:185] op_sel:[0,1] op_sel_hi:[1,0]
	s_nop 0
	v_pk_fma_f32 v[182:183], v[28:29], v[184:185], v[182:183]
	s_nop 0
	v_pk_add_f32 v[180:181], v[180:181], v[182:183]
	v_pk_mul_f32 v[182:183], v[32:33], v[186:187] op_sel:[0,1] op_sel_hi:[1,0]
	s_nop 0
	v_pk_fma_f32 v[182:183], v[36:37], v[186:187], v[182:183]
	s_nop 0
	v_pk_add_f32 v[100:101], v[182:183], v[180:181]
	s_nop 0
	v_pk_add_f32 v[100:101], v[100:101], 0 op_sel_hi:[1,0]
	v_pk_mul_f32 v[96:97], v[38:39], v[188:189] op_sel:[0,1] op_sel_hi:[1,0]
	s_nop 0
	v_pk_fma_f32 v[188:189], v[42:43], v[188:189], v[96:97]
	v_pk_mul_f32 v[96:97], v[46:47], v[190:191] op_sel:[0,1] op_sel_hi:[1,0]
	s_nop 0
	v_pk_fma_f32 v[190:191], v[50:51], v[190:191], v[96:97]
	s_nop 0
	v_pk_add_f32 v[188:189], v[188:189], v[190:191]
	v_pk_mul_f32 v[190:191], v[40:41], v[200:201] op_sel:[0,1] op_sel_hi:[1,0]
	s_nop 0
	v_pk_fma_f32 v[190:191], v[44:45], v[200:201], v[190:191]
	s_nop 0
	v_pk_add_f32 v[102:103], v[188:189], v[190:191]
	v_pk_mul_f32 v[188:189], v[48:49], v[202:203] op_sel:[0,1] op_sel_hi:[1,0]
	s_nop 0
	v_pk_fma_f32 v[104:105], v[52:53], v[202:203], v[188:189]
	s_nop 0
	v_pk_add_f32 v[102:103], v[104:105], v[102:103]
	v_pk_mul_f32 v[96:97], v[54:55], v[204:205] op_sel:[0,1] op_sel_hi:[1,0]
	s_nop 0
	v_pk_fma_f32 v[204:205], v[58:59], v[204:205], v[96:97]
	v_pk_mul_f32 v[96:97], v[62:63], v[206:207] op_sel:[0,1] op_sel_hi:[1,0]
	v_pk_mul_f32 v[108:109], v[68:69], v[210:211]
	v_pk_fma_f32 v[206:207], v[66:67], v[206:207], v[96:97]
	v_pk_fma_f32 v[210:211], v[64:65], v[210:211], v[108:109] op_sel:[0,0,1] op_sel_hi:[1,1,0]
	v_pk_add_f32 v[106:107], v[204:205], v[206:207]
	v_pk_mul_f32 v[204:205], v[56:57], v[208:209] op_sel:[0,1] op_sel_hi:[1,0]
	v_pk_add_f32 v[100:101], v[100:101], v[102:103]
	v_pk_fma_f32 v[208:209], v[60:61], v[208:209], v[204:205]
	s_nop 0
	v_pk_add_f32 v[208:209], v[106:107], v[208:209]
	v_pk_mul_f32 v[110:111], v[70:71], v[212:213] op_sel:[0,1] op_sel_hi:[1,0]
	s_nop 0
	v_pk_fma_f32 v[212:213], v[74:75], v[212:213], v[110:111]
	v_pk_mul_f32 v[110:111], v[78:79], v[214:215] op_sel:[0,1] op_sel_hi:[1,0]
	v_pk_add_f32 v[208:209], v[210:211], v[208:209] op_sel:[0,1] op_sel_hi:[1,0]
	v_pk_fma_f32 v[214:215], v[82:83], v[214:215], v[110:111]
	v_pk_mul_f32 v[110:111], v[76:77], v[92:93]
	v_pk_add_f32 v[212:213], v[212:213], v[214:215]
	v_pk_fma_f32 v[214:215], v[72:73], v[92:93], v[110:111] op_sel:[0,0,1] op_sel_hi:[1,1,0]
	v_pk_add_f32 v[208:209], v[100:101], v[208:209] op_sel:[1,0] op_sel_hi:[0,1]
	v_pk_add_f32 v[212:213], v[212:213], v[214:215] op_sel:[1,0] op_sel_hi:[0,1]
	v_pk_mul_f32 v[214:215], v[84:85], v[94:95]
	s_nop 0
	v_pk_fma_f32 v[214:215], v[80:81], v[94:95], v[214:215] op_sel:[0,0,1] op_sel_hi:[1,1,0]
	s_nop 0
	v_pk_add_f32 v[212:213], v[214:215], v[212:213]
	s_nop 0
	v_pk_add_f32 v[88:89], v[208:209], v[212:213]
	s_nop 1
	v_add_f32_dpp v88, v88, v88 quad_perm:[1,0,3,2] row_mask:0xf bank_mask:0xf
	v_add_f32_dpp v89, v89, v89 quad_perm:[1,0,3,2] row_mask:0xf bank_mask:0xf
	s_nop 0
	v_add_f32_dpp v88, v88, v88 quad_perm:[2,3,0,1] row_mask:0xf bank_mask:0xf
	v_add_f32_dpp v89, v89, v89 quad_perm:[2,3,0,1] row_mask:0xf bank_mask:0xf
	s_nop 0
	v_add_f32_dpp v88, v88, v88 row_half_mirror row_mask:0xf bank_mask:0xf
	v_add_f32_dpp v89, v89, v89 row_half_mirror row_mask:0xf bank_mask:0xf
	s_nop 0
	v_add_f32_dpp v88, v88, v88 row_mirror row_mask:0xf bank_mask:0xf
	v_add_f32_dpp v89, v89, v89 row_mirror row_mask:0xf bank_mask:0xf
	v_mov_b32_e32 v90, v88
	v_mov_b32_e32 v91, v89
	s_nop 1
	v_permlane16_swap_b32_e32 v88, v90
	v_permlane16_swap_b32_e32 v89, v91
	v_add_f32_e32 v88, v88, v90
	v_add_f32_e32 v89, v89, v91
	v_mov_b32_e32 v90, v88
	v_mov_b32_e32 v91, v89
	s_nop 1
	v_permlane32_swap_b32_e32 v88, v90
	v_permlane32_swap_b32_e32 v89, v91
	v_add_f32_e32 v88, v88, v90
	v_add_f32_e32 v89, v89, v91
	v_cndmask_b32_e32 v86, v86, v88, vcc
	v_cndmask_b32_e32 v87, v87, v89, vcc
	s_cmp_lg_u32 s0, 0x20000
	s_cbranch_scc1 .Lmy_rt_loop
; __device__ __forceinline__ void route_row(float mylg, const float* br, int row, int ai0, int lane, LAS int* asg_e, LAS int* asg_d, LAS float* asg_g) {
;     const float myaff = 1.0f / (1.0f + expf(-mylg));
;     float aff[16], sel[16];
; #pragma unroll
;     for (int e = 0; e < 16; ++e) { aff[e] = __shfl(myaff, e); sel[e] = aff[e] + br[e]; }
;     float gs[4];
; #pragma unroll
;     for (int q = 0; q < 4; ++q) { const float s0 = sel[4 * q], s1 = sel[4 * q + 1], s2 = sel[4 * q + 2], s3 = sel[4 * q + 3];
;         gs[q] = fmaxf(fmaxf(fmaxf(s0 + s1, s0 + s2), fmaxf(s0 + s3, s1 + s2)), fmaxf(s1 + s3, s2 + s3)); }
;     int best = 0; float bs = gs[0];
; #pragma unroll
;     for (int q = 1; q < 4; ++q) if (gs[q] > bs) { bs = gs[q]; best = q; }
;     float cs[4], ca[4];
; #pragma unroll
;     for (int i = 0; i < 4; ++i) { cs[i] = best == 0 ? sel[i] : best == 1 ? sel[4 + i] : best == 2 ? sel[8 + i] : sel[12 + i]; ca[i] = best == 0 ? aff[i] : best == 1 ? aff[4 + i] : best == 2 ? aff[8 + i] : aff[12 + i]; }
	s_waitcnt lgkmcnt(0)
	s_andn2_b64 vcc, exec, s[2:3]
	s_cbranch_vccnz .LBB0_838
	v_mul_f32_e32 v2, 0xbfb8aa3b, v87
	v_rndne_f32_e32 v3, v2
	s_mov_b32 s0, 0xbfb8aa3b
	v_sub_f32_e32 v4, v2, v3
	v_fma_f32 v2, v87, s0, -v2
	v_fmac_f32_e32 v2, 0xb2a5705f, v87
	v_add_f32_e32 v2, v4, v2
	v_exp_f32_e32 v2, v2
	v_cvt_i32_f32_e32 v3, v3
	s_mov_b32 s0, 0x42ce8ed0
	v_cmp_nlt_f32_e32 vcc, s0, v87
	s_mov_b32 s0, 0xc2b17218
	v_ldexp_f32 v2, v2, v3
	v_cndmask_b32_e32 v2, 0, v2, vcc
	v_cmp_ngt_f32_e32 vcc, s0, v87
	v_mov_b64_e32 v[52:53], s[28:29]
	s_nop 0
	v_cndmask_b32_e32 v2, v231, v2, vcc
	v_add_f32_e32 v2, 1.0, v2
	v_div_scale_f32 v3, s[0:1], v2, v2, 1.0
	v_rcp_f32_e32 v4, v3
	s_nop 0
	v_fma_f32 v5, -v3, v4, 1.0
	v_fmac_f32_e32 v4, v5, v4
	v_div_scale_f32 v5, vcc, 1.0, v2, 1.0
	v_mul_f32_e32 v26, v5, v4
	v_fma_f32 v27, -v3, v26, v5
	v_fmac_f32_e32 v26, v27, v4
	v_fma_f32 v3, -v3, v26, v5
	v_div_fmas_f32 v3, v3, v4, v26
	v_div_fixup_f32 v56, v3, v2, 1.0
	flat_load_dwordx4 v[2:5], v[52:53]
	ds_bpermute_b32 v28, v124, v56
	ds_bpermute_b32 v29, v126, v56
	ds_bpermute_b32 v34, v128, v56
	ds_bpermute_b32 v35, v130, v56
	ds_bpermute_b32 v38, v127, v56
	ds_bpermute_b32 v39, v129, v56
	ds_bpermute_b32 v42, v131, v56
	ds_bpermute_b32 v43, v133, v56
	ds_bpermute_b32 v26, v123, v56
	ds_bpermute_b32 v27, v125, v56
	ds_bpermute_b32 v46, v135, v56
	ds_bpermute_b32 v47, v137, v56
	s_waitcnt vmcnt(0) lgkmcnt(0)
	v_mov_b32_e32 v31, v4
	v_mov_b32_e32 v4, v3
	v_mov_b32_e32 v30, v2
	v_pk_add_f32 v[32:33], v[4:5], v[28:29]
	flat_load_dwordx4 v[2:5], v[52:53] offset:16
	v_pk_add_f32 v[30:31], v[30:31], v[26:27]
	s_waitcnt vmcnt(0) lgkmcnt(0)
	v_mov_b32_e32 v37, v4
	v_mov_b32_e32 v4, v3
	v_mov_b32_e32 v36, v2
	v_pk_add_f32 v[40:41], v[4:5], v[34:35]
	flat_load_dwordx4 v[2:5], v[52:53] offset:32
	v_pk_add_f32 v[48:49], v[36:37], v[38:39]
	ds_bpermute_b32 v36, v132, v56
	ds_bpermute_b32 v37, v134, v56
	v_add_f32_e32 v57, v32, v31
	v_add_f32_e32 v58, v40, v49
	s_waitcnt vmcnt(0) lgkmcnt(0)
	v_mov_b32_e32 v44, v2
	v_mov_b32_e32 v45, v4
	v_mov_b32_e32 v4, v3
	v_pk_add_f32 v[50:51], v[44:45], v[42:43]
	v_pk_add_f32 v[44:45], v[4:5], v[36:37]
	flat_load_dwordx4 v[2:5], v[52:53] offset:48
	ds_bpermute_b32 v52, v136, v56
	ds_bpermute_b32 v53, v138, v56
	v_add_f32_e32 v56, v30, v31
	v_add_f32_e32 v59, v44, v51
	s_waitcnt vmcnt(0) lgkmcnt(0)
	v_mov_b32_e32 v55, v4
	v_mov_b32_e32 v4, v3
	v_mov_b32_e32 v54, v2
	v_pk_add_f32 v[2:3], v[4:5], v[52:53]
	v_pk_add_f32 v[4:5], v[30:31], v[32:33]
	v_pk_add_f32 v[54:55], v[54:55], v[46:47]
	v_max_f32_e32 v4, v4, v56
	v_add_f32_e32 v56, v30, v33
	v_max_f32_e32 v56, v56, v57
	v_add_f32_e32 v57, v32, v33
	v_max_f32_e32 v5, v57, v5
	v_max3_f32 v56, v4, v56, v5
	v_pk_add_f32 v[4:5], v[48:49], v[40:41]
	v_add_f32_e32 v57, v48, v49
	v_max_f32_e32 v4, v4, v57
	v_add_f32_e32 v57, v48, v41
	v_max_f32_e32 v57, v57, v58
	v_add_f32_e32 v58, v40, v41
	v_max_f32_e32 v5, v58, v5
	v_max3_f32 v57, v4, v57, v5
	v_pk_add_f32 v[4:5], v[50:51], v[44:45]
	v_add_f32_e32 v58, v50, v51
	v_max_f32_e32 v4, v4, v58
	v_add_f32_e32 v58, v50, v45
	v_max_f32_e32 v58, v58, v59
	v_add_f32_e32 v59, v44, v45
	v_max_f32_e32 v5, v59, v5
	v_max3_f32 v58, v4, v58, v5
	v_pk_add_f32 v[4:5], v[54:55], v[2:3]
	v_add_f32_e32 v59, v54, v55
	v_max_f32_e32 v4, v4, v59
	v_add_f32_e32 v59, v54, v3
	v_add_f32_e32 v60, v2, v55
	v_max_f32_e32 v59, v59, v60
	v_add_f32_e32 v60, v2, v3
	v_cmp_gt_f32_e32 vcc, v57, v56
	v_max_f32_e32 v5, v60, v5
	v_max3_f32 v4, v4, v59, v5
	v_cndmask_b32_e32 v56, v56, v57, vcc
	v_cndmask_b32_e64 v5, 0, 1, vcc
	v_cmp_gt_f32_e32 vcc, v58, v56
	s_nop 1
	v_cndmask_b32_e32 v56, v56, v58, vcc
	v_cndmask_b32_e64 v5, v5, 2, vcc
	v_cmp_ngt_f32_e32 vcc, v4, v56
	s_nop 1
	v_cndmask_b32_e32 v4, 3, v5, vcc
	v_cmp_ne_u32_e32 vcc, 0, v4
	s_and_saveexec_b64 s[2:3], vcc
	s_cbranch_execz .LBB0_879
	v_cmp_lt_i32_e64 s[0:1], 1, v4
	s_and_saveexec_b64 s[10:11], s[0:1]
	s_cbranch_execz .LBB0_816
	v_cmp_ne_u32_e64 s[0:1], 2, v4
	v_mov_b32_e32 v48, v50
	s_and_saveexec_b64 s[8:9], s[0:1]
	s_xor_b64 s[0:1], exec, s[8:9]
	v_mov_b32_e32 v48, v54
	s_andn2_saveexec_b64 s[0:1], s[0:1]
	s_or_b64 exec, exec, s[0:1]
